# dilated attention: lower band edge handled by -inf entries of the bias table, explicit masks only on causal-edge tiles
# baseline (speedup 1.0000x reference)
.LBB0_1560:
	s_cmp_eq_u32 s63, 3
	s_cselect_b64 s[12:13], -1, 0
	s_cmp_eq_u32 s62, 3
	s_cselect_b64 s[46:47], -1, 0
	s_and_b64 s[12:13], s[12:13], s[46:47]
	s_and_b64 vcc, exec, s[12:13]
	s_cbranch_vccnz .LBB0_1566
	s_lshl_b32 s12, s61, 6
	s_add_i32 s12, s12, s51
	s_lshl_b32 s12, s12, 2
	v_subrev_u32_e32 v2, s12, v143
	ds_read2_b32 v[146:147], v2 offset0:127 offset1:128
	s_cmp_eq_u32 s62, 1
	s_cselect_b32 s12, 1, 0
	s_cmp_eq_u32 s63, 1
	s_cselect_b32 s12, 1, s12
	s_cmp_eq_u32 s12, 0
	s_waitcnt lgkmcnt(0)
	v_pk_add_f32 v[68:69], v[68:69], v[146:147] op_sel:[0,1] op_sel_hi:[1,0]
	ds_read2_b32 v[146:147], v2 offset0:95 offset1:96
	s_waitcnt lgkmcnt(0)
	v_pk_add_f32 v[36:37], v[36:37], v[146:147] op_sel:[0,1] op_sel_hi:[1,0]
	ds_read2_b32 v[146:147], v2 offset0:125 offset1:126
	s_waitcnt lgkmcnt(0)
	v_pk_add_f32 v[70:71], v[70:71], v[146:147] op_sel:[0,1] op_sel_hi:[1,0]
	ds_read2_b32 v[146:147], v2 offset0:93 offset1:94
	s_waitcnt lgkmcnt(0)
	v_pk_add_f32 v[38:39], v[38:39], v[146:147] op_sel:[0,1] op_sel_hi:[1,0]
	ds_read2_b32 v[146:147], v2 offset0:119 offset1:120
	s_waitcnt lgkmcnt(0)
	v_pk_add_f32 v[72:73], v[72:73], v[146:147] op_sel:[0,1] op_sel_hi:[1,0]
	ds_read2_b32 v[146:147], v2 offset0:87 offset1:88
	s_waitcnt lgkmcnt(0)
	v_pk_add_f32 v[40:41], v[40:41], v[146:147] op_sel:[0,1] op_sel_hi:[1,0]
	ds_read2_b32 v[146:147], v2 offset0:117 offset1:118
	s_waitcnt lgkmcnt(0)
	v_pk_add_f32 v[74:75], v[74:75], v[146:147] op_sel:[0,1] op_sel_hi:[1,0]
	ds_read2_b32 v[146:147], v2 offset0:85 offset1:86
	s_waitcnt lgkmcnt(0)
	v_pk_add_f32 v[42:43], v[42:43], v[146:147] op_sel:[0,1] op_sel_hi:[1,0]
	ds_read2_b32 v[146:147], v2 offset0:111 offset1:112
	s_waitcnt lgkmcnt(0)
	v_pk_add_f32 v[76:77], v[76:77], v[146:147] op_sel:[0,1] op_sel_hi:[1,0]
	ds_read2_b32 v[146:147], v2 offset0:79 offset1:80
	s_waitcnt lgkmcnt(0)
	v_pk_add_f32 v[44:45], v[44:45], v[146:147] op_sel:[0,1] op_sel_hi:[1,0]
	ds_read2_b32 v[146:147], v2 offset0:109 offset1:110
	s_waitcnt lgkmcnt(0)
	v_pk_add_f32 v[78:79], v[78:79], v[146:147] op_sel:[0,1] op_sel_hi:[1,0]
	ds_read2_b32 v[146:147], v2 offset0:77 offset1:78
	s_waitcnt lgkmcnt(0)
	v_pk_add_f32 v[46:47], v[46:47], v[146:147] op_sel:[0,1] op_sel_hi:[1,0]
	ds_read2_b32 v[146:147], v2 offset0:103 offset1:104
	s_waitcnt lgkmcnt(0)
	v_pk_add_f32 v[80:81], v[80:81], v[146:147] op_sel:[0,1] op_sel_hi:[1,0]
	ds_read2_b32 v[146:147], v2 offset0:71 offset1:72
	s_waitcnt lgkmcnt(0)
	v_pk_add_f32 v[48:49], v[48:49], v[146:147] op_sel:[0,1] op_sel_hi:[1,0]
	ds_read2_b32 v[146:147], v2 offset0:101 offset1:102
	s_waitcnt lgkmcnt(0)
	v_pk_add_f32 v[82:83], v[82:83], v[146:147] op_sel:[0,1] op_sel_hi:[1,0]
	ds_read2_b32 v[146:147], v2 offset0:69 offset1:70
	s_waitcnt lgkmcnt(0)
	v_pk_add_f32 v[50:51], v[50:51], v[146:147] op_sel:[0,1] op_sel_hi:[1,0]
	s_cbranch_scc1 .LBB0_1563
	s_cmp_eq_u32 s63, 2
	s_cselect_b64 vcc, -1, 0
	s_cmp_eq_u32 s63, 1
	s_cselect_b64 s[12:13], -1, 0
	s_cmp_eq_u32 s63, 3
	s_cselect_b32 s46, 64, 0
	v_mov_b32_e32 v2, s46
	s_cselect_b32 s46, -1, 63
	s_cmp_eq_u32 s62, 2
	v_cndmask_b32_e32 v2, v2, v138, vcc
	v_mov_b32_e32 v146, s46
	s_cselect_b64 vcc, -1, 0
	s_cmp_eq_u32 s62, 1
	v_cndmask_b32_e64 v146, v146, v138, s[12:13]
	s_cselect_b64 s[12:13], -1, 0
	s_cmp_eq_u32 s62, 3
	s_cselect_b32 s46, 64, 0
	v_mov_b32_e32 v147, s46
	s_cselect_b32 s46, -1, 63
	v_sub_u32_e32 v2, v2, v141
	v_sub_u32_e32 v146, v146, v141
	v_mov_b32_e32 v148, s46
	v_cndmask_b32_e32 v147, v147, v138, vcc
	v_cndmask_b32_e64 v148, v148, v138, s[12:13]
	v_cmp_lt_i32_e32 vcc, 0, v2
	v_cmp_gt_i32_e64 s[12:13], 0, v146
	v_sub_u32_e32 v147, v147, v141
	v_sub_u32_e32 v148, v148, v141
	s_or_b64 vcc, vcc, s[12:13]
	v_cndmask_b32_e32 v68, v68, v234, vcc
	v_cmp_lt_i32_e32 vcc, 0, v147
	v_cmp_gt_i32_e64 s[12:13], 0, v148
	s_or_b64 vcc, vcc, s[12:13]
	v_cndmask_b32_e32 v36, v36, v234, vcc
	v_cmp_lt_i32_e32 vcc, 1, v2
	v_cmp_gt_i32_e64 s[12:13], 1, v146
	s_or_b64 vcc, vcc, s[12:13]
	v_cndmask_b32_e32 v69, v69, v234, vcc
	v_cmp_lt_i32_e32 vcc, 1, v147
	v_cmp_gt_i32_e64 s[12:13], 1, v148
	s_or_b64 vcc, vcc, s[12:13]
	v_cndmask_b32_e32 v37, v37, v234, vcc
	v_cmp_lt_i32_e32 vcc, 2, v2
	v_cmp_gt_i32_e64 s[12:13], 2, v146
	s_or_b64 vcc, vcc, s[12:13]
	v_cndmask_b32_e32 v70, v70, v234, vcc
	v_cmp_lt_i32_e32 vcc, 2, v147
	v_cmp_gt_i32_e64 s[12:13], 2, v148
	s_or_b64 vcc, vcc, s[12:13]
	v_cndmask_b32_e32 v38, v38, v234, vcc
	v_cmp_lt_i32_e32 vcc, 3, v2
	v_cmp_gt_i32_e64 s[12:13], 3, v146
	s_or_b64 vcc, vcc, s[12:13]
	v_cndmask_b32_e32 v71, v71, v234, vcc
	v_cmp_lt_i32_e32 vcc, 3, v147
	v_cmp_gt_i32_e64 s[12:13], 3, v148
	s_or_b64 vcc, vcc, s[12:13]
	v_cndmask_b32_e32 v39, v39, v234, vcc
	v_cmp_lt_i32_e32 vcc, 8, v2
	v_cmp_gt_i32_e64 s[12:13], 8, v146
	s_or_b64 vcc, vcc, s[12:13]
	v_cndmask_b32_e32 v72, v72, v234, vcc
	v_cmp_lt_i32_e32 vcc, 8, v147
	v_cmp_gt_i32_e64 s[12:13], 8, v148
	s_or_b64 vcc, vcc, s[12:13]
	v_cndmask_b32_e32 v40, v40, v234, vcc
	v_cmp_lt_i32_e32 vcc, 9, v2
	v_cmp_gt_i32_e64 s[12:13], 9, v146
	s_or_b64 vcc, vcc, s[12:13]
	v_cndmask_b32_e32 v73, v73, v234, vcc
	v_cmp_lt_i32_e32 vcc, 9, v147
	v_cmp_gt_i32_e64 s[12:13], 9, v148
	s_or_b64 vcc, vcc, s[12:13]
	v_cndmask_b32_e32 v41, v41, v234, vcc
	v_cmp_lt_i32_e32 vcc, 10, v2
	v_cmp_gt_i32_e64 s[12:13], 10, v146
	s_or_b64 vcc, vcc, s[12:13]
	v_cndmask_b32_e32 v74, v74, v234, vcc
	v_cmp_lt_i32_e32 vcc, 10, v147
	v_cmp_gt_i32_e64 s[12:13], 10, v148
	s_or_b64 vcc, vcc, s[12:13]
	v_cndmask_b32_e32 v42, v42, v234, vcc
	v_cmp_lt_i32_e32 vcc, 11, v2
	v_cmp_gt_i32_e64 s[12:13], 11, v146
	s_or_b64 vcc, vcc, s[12:13]
	v_cndmask_b32_e32 v75, v75, v234, vcc
	v_cmp_lt_i32_e32 vcc, 11, v147
	v_cmp_gt_i32_e64 s[12:13], 11, v148
	s_or_b64 vcc, vcc, s[12:13]
	v_cndmask_b32_e32 v43, v43, v234, vcc
	v_cmp_lt_i32_e32 vcc, 16, v2
	v_cmp_gt_i32_e64 s[12:13], 16, v146
	s_or_b64 vcc, vcc, s[12:13]
	v_cndmask_b32_e32 v76, v76, v234, vcc
	v_cmp_lt_i32_e32 vcc, 16, v147
	v_cmp_gt_i32_e64 s[12:13], 16, v148
	s_or_b64 vcc, vcc, s[12:13]
	v_cndmask_b32_e32 v44, v44, v234, vcc
	v_cmp_lt_i32_e32 vcc, 17, v2
	v_cmp_gt_i32_e64 s[12:13], 17, v146
	s_or_b64 vcc, vcc, s[12:13]
	v_cndmask_b32_e32 v77, v77, v234, vcc
	v_cmp_lt_i32_e32 vcc, 17, v147
	v_cmp_gt_i32_e64 s[12:13], 17, v148
	s_or_b64 vcc, vcc, s[12:13]
	v_cndmask_b32_e32 v45, v45, v234, vcc
	v_cmp_lt_i32_e32 vcc, 18, v2
	v_cmp_gt_i32_e64 s[12:13], 18, v146
	s_or_b64 vcc, vcc, s[12:13]
	v_cndmask_b32_e32 v78, v78, v234, vcc
	v_cmp_lt_i32_e32 vcc, 18, v147
	v_cmp_gt_i32_e64 s[12:13], 18, v148
	s_or_b64 vcc, vcc, s[12:13]
	v_cndmask_b32_e32 v46, v46, v234, vcc
	v_cmp_lt_i32_e32 vcc, 19, v2
	v_cmp_gt_i32_e64 s[12:13], 19, v146
	s_or_b64 vcc, vcc, s[12:13]
	v_cndmask_b32_e32 v79, v79, v234, vcc
	v_cmp_lt_i32_e32 vcc, 19, v147
	v_cmp_gt_i32_e64 s[12:13], 19, v148
	s_or_b64 vcc, vcc, s[12:13]
	v_cndmask_b32_e32 v47, v47, v234, vcc
	v_cmp_lt_i32_e32 vcc, 24, v2
	v_cmp_gt_i32_e64 s[12:13], 24, v146
	s_or_b64 vcc, vcc, s[12:13]
	v_cndmask_b32_e32 v80, v80, v234, vcc
	v_cmp_lt_i32_e32 vcc, 24, v147
	v_cmp_gt_i32_e64 s[12:13], 24, v148
	s_or_b64 vcc, vcc, s[12:13]
	v_cndmask_b32_e32 v48, v48, v234, vcc
	v_cmp_lt_i32_e32 vcc, 25, v2
	v_cmp_gt_i32_e64 s[12:13], 25, v146
	s_or_b64 vcc, vcc, s[12:13]
	v_cndmask_b32_e32 v81, v81, v234, vcc
	v_cmp_lt_i32_e32 vcc, 25, v147
	v_cmp_gt_i32_e64 s[12:13], 25, v148
	s_or_b64 vcc, vcc, s[12:13]
	v_cndmask_b32_e32 v49, v49, v234, vcc
	v_cmp_lt_i32_e32 vcc, 26, v2
	v_cmp_gt_i32_e64 s[12:13], 26, v146
	s_or_b64 vcc, vcc, s[12:13]
	v_cndmask_b32_e32 v82, v82, v234, vcc
	v_cmp_lt_i32_e32 vcc, 26, v147
	v_cmp_gt_i32_e64 s[12:13], 26, v148
	s_or_b64 vcc, vcc, s[12:13]
	v_cndmask_b32_e32 v50, v50, v234, vcc
	v_cmp_lt_i32_e32 vcc, 27, v2
	v_cmp_gt_i32_e64 s[12:13], 27, v146
	s_or_b64 vcc, vcc, s[12:13]
	v_cndmask_b32_e32 v83, v83, v234, vcc
	v_cmp_lt_i32_e32 vcc, 27, v147
	v_cmp_gt_i32_e64 s[12:13], 27, v148
	s_or_b64 vcc, vcc, s[12:13]
	v_cndmask_b32_e32 v51, v51, v234, vcc

.LBB0_1588:
	s_cmp_eq_u32 s60, 3
	s_cselect_b64 s[12:13], -1, 0
	s_cmp_eq_u32 s47, 3
	s_cselect_b64 s[40:41], -1, 0
	s_and_b64 s[12:13], s[12:13], s[40:41]
	s_and_b64 vcc, exec, s[12:13]
	s_cbranch_vccnz .LBB0_1594
	s_lshl_b32 s12, s59, 6
	s_add_i32 s12, s12, s51
	s_lshl_b32 s12, s12, 2
	v_subrev_u32_e32 v145, s12, v143
	ds_read2_b32 v[146:147], v145 offset0:127 offset1:128
	s_cmp_eq_u32 s47, 1
	s_cselect_b32 s12, 1, 0
	s_cmp_eq_u32 s60, 1
	s_cselect_b32 s12, 1, s12
	s_cmp_eq_u32 s12, 0
	s_waitcnt lgkmcnt(0)
	v_pk_add_f32 v[84:85], v[84:85], v[146:147] op_sel:[0,1] op_sel_hi:[1,0]
	ds_read2_b32 v[146:147], v145 offset0:95 offset1:96
	s_waitcnt lgkmcnt(0)
	v_pk_add_f32 v[100:101], v[100:101], v[146:147] op_sel:[0,1] op_sel_hi:[1,0]
	ds_read2_b32 v[146:147], v145 offset0:125 offset1:126
	s_waitcnt lgkmcnt(0)
	v_pk_add_f32 v[86:87], v[86:87], v[146:147] op_sel:[0,1] op_sel_hi:[1,0]
	ds_read2_b32 v[146:147], v145 offset0:93 offset1:94
	s_waitcnt lgkmcnt(0)
	v_pk_add_f32 v[102:103], v[102:103], v[146:147] op_sel:[0,1] op_sel_hi:[1,0]
	ds_read2_b32 v[146:147], v145 offset0:119 offset1:120
	s_waitcnt lgkmcnt(0)
	v_pk_add_f32 v[88:89], v[88:89], v[146:147] op_sel:[0,1] op_sel_hi:[1,0]
	ds_read2_b32 v[146:147], v145 offset0:87 offset1:88
	s_waitcnt lgkmcnt(0)
	v_pk_add_f32 v[104:105], v[104:105], v[146:147] op_sel:[0,1] op_sel_hi:[1,0]
	ds_read2_b32 v[146:147], v145 offset0:117 offset1:118
	s_waitcnt lgkmcnt(0)
	v_pk_add_f32 v[90:91], v[90:91], v[146:147] op_sel:[0,1] op_sel_hi:[1,0]
	ds_read2_b32 v[146:147], v145 offset0:85 offset1:86
	s_waitcnt lgkmcnt(0)
	v_pk_add_f32 v[106:107], v[106:107], v[146:147] op_sel:[0,1] op_sel_hi:[1,0]
	ds_read2_b32 v[146:147], v145 offset0:111 offset1:112
	s_waitcnt lgkmcnt(0)
	v_pk_add_f32 v[92:93], v[92:93], v[146:147] op_sel:[0,1] op_sel_hi:[1,0]
	ds_read2_b32 v[146:147], v145 offset0:79 offset1:80
	s_waitcnt lgkmcnt(0)
	v_pk_add_f32 v[108:109], v[108:109], v[146:147] op_sel:[0,1] op_sel_hi:[1,0]
	ds_read2_b32 v[146:147], v145 offset0:109 offset1:110
	s_waitcnt lgkmcnt(0)
	v_pk_add_f32 v[94:95], v[94:95], v[146:147] op_sel:[0,1] op_sel_hi:[1,0]
	ds_read2_b32 v[146:147], v145 offset0:77 offset1:78
	s_waitcnt lgkmcnt(0)
	v_pk_add_f32 v[110:111], v[110:111], v[146:147] op_sel:[0,1] op_sel_hi:[1,0]
	ds_read2_b32 v[146:147], v145 offset0:103 offset1:104
	s_waitcnt lgkmcnt(0)
	v_pk_add_f32 v[96:97], v[96:97], v[146:147] op_sel:[0,1] op_sel_hi:[1,0]
	ds_read2_b32 v[146:147], v145 offset0:71 offset1:72
	s_waitcnt lgkmcnt(0)
	v_pk_add_f32 v[112:113], v[112:113], v[146:147] op_sel:[0,1] op_sel_hi:[1,0]
	ds_read2_b32 v[146:147], v145 offset0:101 offset1:102
	s_waitcnt lgkmcnt(0)
	v_pk_add_f32 v[98:99], v[98:99], v[146:147] op_sel:[0,1] op_sel_hi:[1,0]
	ds_read2_b32 v[146:147], v145 offset0:69 offset1:70
	s_waitcnt lgkmcnt(0)
	v_pk_add_f32 v[114:115], v[114:115], v[146:147] op_sel:[0,1] op_sel_hi:[1,0]
	s_cbranch_scc1 .LBB0_1591
	s_cmp_eq_u32 s60, 2
	s_cselect_b64 vcc, -1, 0
	s_cmp_eq_u32 s60, 1
	s_cselect_b64 s[12:13], -1, 0
	s_cmp_eq_u32 s60, 3
	s_cselect_b32 s40, 64, 0
	v_mov_b32_e32 v145, s40
	s_cselect_b32 s40, -1, 63
	s_cmp_eq_u32 s47, 2
	v_cndmask_b32_e32 v145, v145, v138, vcc
	v_mov_b32_e32 v146, s40
	s_cselect_b64 vcc, -1, 0
	s_cmp_eq_u32 s47, 1
	v_cndmask_b32_e64 v146, v146, v138, s[12:13]
	s_cselect_b64 s[12:13], -1, 0
	s_cmp_eq_u32 s47, 3
	s_cselect_b32 s40, 64, 0
	v_mov_b32_e32 v147, s40
	s_cselect_b32 s40, -1, 63
	v_sub_u32_e32 v145, v145, v141
	v_sub_u32_e32 v146, v146, v141
	v_mov_b32_e32 v148, s40
	v_cndmask_b32_e32 v147, v147, v138, vcc
	v_cndmask_b32_e64 v148, v148, v138, s[12:13]
	v_cmp_lt_i32_e32 vcc, 0, v145
	v_cmp_gt_i32_e64 s[12:13], 0, v146
	v_sub_u32_e32 v147, v147, v141
	v_sub_u32_e32 v148, v148, v141
	s_or_b64 vcc, vcc, s[12:13]
	v_cndmask_b32_e32 v84, v84, v234, vcc
	v_cmp_lt_i32_e32 vcc, 0, v147
	v_cmp_gt_i32_e64 s[12:13], 0, v148
	s_or_b64 vcc, vcc, s[12:13]
	v_cndmask_b32_e32 v100, v100, v234, vcc
	v_cmp_lt_i32_e32 vcc, 1, v145
	v_cmp_gt_i32_e64 s[12:13], 1, v146
	s_or_b64 vcc, vcc, s[12:13]
	v_cndmask_b32_e32 v85, v85, v234, vcc
	v_cmp_lt_i32_e32 vcc, 1, v147
	v_cmp_gt_i32_e64 s[12:13], 1, v148
	s_or_b64 vcc, vcc, s[12:13]
	v_cndmask_b32_e32 v101, v101, v234, vcc
	v_cmp_lt_i32_e32 vcc, 2, v145
	v_cmp_gt_i32_e64 s[12:13], 2, v146
	s_or_b64 vcc, vcc, s[12:13]
	v_cndmask_b32_e32 v86, v86, v234, vcc
	v_cmp_lt_i32_e32 vcc, 2, v147
	v_cmp_gt_i32_e64 s[12:13], 2, v148
	s_or_b64 vcc, vcc, s[12:13]
	v_cndmask_b32_e32 v102, v102, v234, vcc
	v_cmp_lt_i32_e32 vcc, 3, v145
	v_cmp_gt_i32_e64 s[12:13], 3, v146
	s_or_b64 vcc, vcc, s[12:13]
	v_cndmask_b32_e32 v87, v87, v234, vcc
	v_cmp_lt_i32_e32 vcc, 3, v147
	v_cmp_gt_i32_e64 s[12:13], 3, v148
	s_or_b64 vcc, vcc, s[12:13]
	v_cndmask_b32_e32 v103, v103, v234, vcc
	v_cmp_lt_i32_e32 vcc, 8, v145
	v_cmp_gt_i32_e64 s[12:13], 8, v146
	s_or_b64 vcc, vcc, s[12:13]
	v_cndmask_b32_e32 v88, v88, v234, vcc
	v_cmp_lt_i32_e32 vcc, 8, v147
	v_cmp_gt_i32_e64 s[12:13], 8, v148
	s_or_b64 vcc, vcc, s[12:13]
	v_cndmask_b32_e32 v104, v104, v234, vcc
	v_cmp_lt_i32_e32 vcc, 9, v145
	v_cmp_gt_i32_e64 s[12:13], 9, v146
	s_or_b64 vcc, vcc, s[12:13]
	v_cndmask_b32_e32 v89, v89, v234, vcc
	v_cmp_lt_i32_e32 vcc, 9, v147
	v_cmp_gt_i32_e64 s[12:13], 9, v148
	s_or_b64 vcc, vcc, s[12:13]
	v_cndmask_b32_e32 v105, v105, v234, vcc
	v_cmp_lt_i32_e32 vcc, 10, v145
	v_cmp_gt_i32_e64 s[12:13], 10, v146
	s_or_b64 vcc, vcc, s[12:13]
	v_cndmask_b32_e32 v90, v90, v234, vcc
	v_cmp_lt_i32_e32 vcc, 10, v147
	v_cmp_gt_i32_e64 s[12:13], 10, v148
	s_or_b64 vcc, vcc, s[12:13]
	v_cndmask_b32_e32 v106, v106, v234, vcc
	v_cmp_lt_i32_e32 vcc, 11, v145
	v_cmp_gt_i32_e64 s[12:13], 11, v146
	s_or_b64 vcc, vcc, s[12:13]
	v_cndmask_b32_e32 v91, v91, v234, vcc
	v_cmp_lt_i32_e32 vcc, 11, v147
	v_cmp_gt_i32_e64 s[12:13], 11, v148
	s_or_b64 vcc, vcc, s[12:13]
	v_cndmask_b32_e32 v107, v107, v234, vcc
	v_cmp_lt_i32_e32 vcc, 16, v145
	v_cmp_gt_i32_e64 s[12:13], 16, v146
	s_or_b64 vcc, vcc, s[12:13]
	v_cndmask_b32_e32 v92, v92, v234, vcc
	v_cmp_lt_i32_e32 vcc, 16, v147
	v_cmp_gt_i32_e64 s[12:13], 16, v148
	s_or_b64 vcc, vcc, s[12:13]
	v_cndmask_b32_e32 v108, v108, v234, vcc
	v_cmp_lt_i32_e32 vcc, 17, v145
	v_cmp_gt_i32_e64 s[12:13], 17, v146
	s_or_b64 vcc, vcc, s[12:13]
	v_cndmask_b32_e32 v93, v93, v234, vcc
	v_cmp_lt_i32_e32 vcc, 17, v147
	v_cmp_gt_i32_e64 s[12:13], 17, v148
	s_or_b64 vcc, vcc, s[12:13]
	v_cndmask_b32_e32 v109, v109, v234, vcc
	v_cmp_lt_i32_e32 vcc, 18, v145
	v_cmp_gt_i32_e64 s[12:13], 18, v146
	s_or_b64 vcc, vcc, s[12:13]
	v_cndmask_b32_e32 v94, v94, v234, vcc
	v_cmp_lt_i32_e32 vcc, 18, v147
	v_cmp_gt_i32_e64 s[12:13], 18, v148
	s_or_b64 vcc, vcc, s[12:13]
	v_cndmask_b32_e32 v110, v110, v234, vcc
	v_cmp_lt_i32_e32 vcc, 19, v145
	v_cmp_gt_i32_e64 s[12:13], 19, v146
	s_or_b64 vcc, vcc, s[12:13]
	v_cndmask_b32_e32 v95, v95, v234, vcc
	v_cmp_lt_i32_e32 vcc, 19, v147
	v_cmp_gt_i32_e64 s[12:13], 19, v148
	s_or_b64 vcc, vcc, s[12:13]
	v_cndmask_b32_e32 v111, v111, v234, vcc
	v_cmp_lt_i32_e32 vcc, 24, v145
	v_cmp_gt_i32_e64 s[12:13], 24, v146
	s_or_b64 vcc, vcc, s[12:13]
	v_cndmask_b32_e32 v96, v96, v234, vcc
	v_cmp_lt_i32_e32 vcc, 24, v147
	v_cmp_gt_i32_e64 s[12:13], 24, v148
	s_or_b64 vcc, vcc, s[12:13]
	v_cndmask_b32_e32 v112, v112, v234, vcc
	v_cmp_lt_i32_e32 vcc, 25, v145
	v_cmp_gt_i32_e64 s[12:13], 25, v146
	s_or_b64 vcc, vcc, s[12:13]
	v_cndmask_b32_e32 v97, v97, v234, vcc
	v_cmp_lt_i32_e32 vcc, 25, v147
	v_cmp_gt_i32_e64 s[12:13], 25, v148
	s_or_b64 vcc, vcc, s[12:13]
	v_cndmask_b32_e32 v113, v113, v234, vcc
	v_cmp_lt_i32_e32 vcc, 26, v145
	v_cmp_gt_i32_e64 s[12:13], 26, v146
	s_or_b64 vcc, vcc, s[12:13]
	v_cndmask_b32_e32 v98, v98, v234, vcc
	v_cmp_lt_i32_e32 vcc, 26, v147
	v_cmp_gt_i32_e64 s[12:13], 26, v148
	s_or_b64 vcc, vcc, s[12:13]
	v_cndmask_b32_e32 v114, v114, v234, vcc
	v_cmp_lt_i32_e32 vcc, 27, v145
	v_cmp_gt_i32_e64 s[12:13], 27, v146
	s_or_b64 vcc, vcc, s[12:13]
	v_cndmask_b32_e32 v99, v99, v234, vcc
	v_cmp_lt_i32_e32 vcc, 27, v147
	v_cmp_gt_i32_e64 s[12:13], 27, v148
	s_or_b64 vcc, vcc, s[12:13]
	v_cndmask_b32_e32 v115, v115, v234, vcc
